# GEMM k-loops: the eight back-to-back s_setprio 0 / s_setprio 1 pairs between the two halves of each MFMA cluster deleted
# baseline (speedup 1.0000x reference)
; #define PG8_STAGE(bufoff, gbase, voff) do { _Pragma("unroll") for (int _i = 0; _i < 2; ++_i) \
;         __builtin_amdgcn_global_load_lds((const unsigned*)((const char*)(gbase) + (voff)[_i]), (PG8_LAS unsigned*)(lds + (bufoff) + ldsw + _i * 8192), 16, 0, 0); } while (0)
; #define PG8_STAGE_A(bufoff, gb, vo, h) do { if constexpr (Sched::GATHER) { PG8_STAGE(bufoff, gb, (vo)[h]); } else { PG8_STAGE(bufoff, (gb) + (h) * hstep, voffA); } } while (0)
; #define PG8_LDA(dst, b, h) do { _Pragma("unroll") for (int m = 0; m < 4; ++m) _Pragma("unroll") for (int k = 0; k < 2; ++k) dst[m][k] = *(const PG8_LAS bf16x8*)(lds + PG8_SA(b, h) + aoff + m * 2048 + k * 1024); } while (0)
; #define PG8_LDB(dst, b, h) do { _Pragma("unroll") for (int n = 0; n < 2; ++n) _Pragma("unroll") for (int k = 0; k < 2; ++k) dst[n][k] = *(const PG8_LAS bf16x8*)(lds + PG8_SB(b, h) + boff + n * 2048 + k * 1024); } while (0)
; #define PG8_MMA(ai, bj, At, Bt) do { __builtin_amdgcn_s_setprio(1); _Pragma("unroll") for (int m = 0; m < 4; ++m) _Pragma("unroll") for (int n = 0; n < 2; ++n) _Pragma("unroll") for (int k = 0; k < 2; ++k) \
;         acc[ai][bj][m][n] = __builtin_amdgcn_mfma_f32_16x16x32_bf16(Bt[n][k], At[m][k], acc[ai][bj][m][n], 0, 0, 0); __builtin_amdgcn_s_setprio(0); } while (0)
; #define PG8_WAIT_V(n) asm volatile("s_waitcnt vmcnt(" #n ")" ::: "memory")
; #define PG8_WAIT_L(n) asm volatile("s_waitcnt lgkmcnt(" #n ")" ::: "memory")
; #define PG8_BAR __builtin_amdgcn_s_barrier()
; #define PG8_SCHED __builtin_amdgcn_sched_barrier(0)
; template <class Epi, class Sched, bool ALIGN_EPI>
; __device__ __forceinline__ void gemm_phase(PG8_LAS unsigned char* lds, const int K, const Sched& S, const Epi& E) {
;     ...
;             PG8_LDB(B0, 0, 0); PG8_LDB(B1, 0, 1); PG8_SCHED; PG8_LDA(At, 0, 0); PG8_STAGE_A(PG8_SA(1, 1), a1, cvo, 1);
;             PG8_WAIT_V(8); PG8_WAIT_L(0); PG8_BAR; PG8_MMA(0, 0, At, B0); PG8_MMA(0, 1, At, B1); PG8_BAR; PG8_SCHED;
;             PG8_LDA(At, 0, 1); PG8_STAGE(PG8_SB(0, 0), b2, voffB); PG8_STAGE(PG8_SB(0, 1), b2 + hstep, voffB); PG8_STAGE_A(PG8_SA(0, 0), a2, vo2, 0);
;             PG8_WAIT_V(8); PG8_WAIT_L(0); PG8_BAR; PG8_MMA(1, 0, At, B0); PG8_MMA(1, 1, At, B1); PG8_BAR; PG8_SCHED;
.LBB0_199:
	ds_read_b128 v[148:151], v156
	ds_read_b128 v[160:163], v156 offset:1024
	ds_read_b128 v[164:167], v156 offset:2048
	ds_read_b128 v[168:171], v156 offset:3072
	ds_read_b128 v[172:175], v157
	ds_read_b128 v[176:179], v157 offset:1024
	ds_read_b128 v[180:183], v157 offset:2048
	ds_read_b128 v[184:187], v157 offset:3072
	s_add_u32 s24, s22, 0xfff00080
	s_addc_u32 s25, s23, -1
	s_cmp_eq_u32 s50, 60
	s_cselect_b32 s27, s15, s25
	s_cselect_b32 s26, s46, s24
	s_cselect_b32 s25, s13, s49
	s_cselect_b32 s24, s47, s48
	v_lshl_add_u64 v[220:221], s[22:23], 0, v[140:141]
	s_add_i32 m0, s21, 0xc000
	ds_read_b128 v[188:191], v158
	ds_read_b128 v[192:195], v158 offset:1024
	ds_read_b128 v[196:199], v158 offset:2048
	ds_read_b128 v[200:203], v158 offset:3072
	ds_read_b128 v[204:207], v158 offset:4096
	ds_read_b128 v[208:211], v158 offset:5120
	ds_read_b128 v[212:215], v158 offset:6144
	ds_read_b128 v[216:219], v158 offset:7168
	global_load_lds_dwordx4 v[220:221], off
	v_lshl_add_u64 v[220:221], s[22:23], 0, v[142:143]
	s_add_i32 m0, s21, 0xe000
	s_nop 0
	global_load_lds_dwordx4 v[220:221], off
	s_waitcnt vmcnt(8)
	s_waitcnt lgkmcnt(0)
	s_barrier
	s_setprio 1
	s_waitcnt lgkmcnt(0)
	v_mfma_f32_16x16x32_bf16 v[126:129], v[148:151], v[188:191], v[126:129]
	v_mfma_f32_16x16x32_bf16 v[122:125], v[164:167], v[188:191], v[122:125]
	v_mfma_f32_16x16x32_bf16 v[118:121], v[148:151], v[196:199], v[118:121]
	v_mfma_f32_16x16x32_bf16 v[110:113], v[164:167], v[196:199], v[110:113]
	v_mfma_f32_16x16x32_bf16 v[102:105], v[148:151], v[204:207], v[102:105]
	v_mfma_f32_16x16x32_bf16 v[94:97], v[164:167], v[204:207], v[94:97]
	v_mfma_f32_16x16x32_bf16 v[86:89], v[148:151], v[212:215], v[86:89]
	v_mfma_f32_16x16x32_bf16 v[78:81], v[164:167], v[212:215], v[78:81]
	v_mfma_f32_16x16x32_bf16 v[126:129], v[160:163], v[192:195], v[126:129]
	v_mfma_f32_16x16x32_bf16 v[122:125], v[168:171], v[192:195], v[122:125]
	v_mfma_f32_16x16x32_bf16 v[118:121], v[160:163], v[200:203], v[118:121]
	v_mfma_f32_16x16x32_bf16 v[110:113], v[168:171], v[200:203], v[110:113]
	v_mfma_f32_16x16x32_bf16 v[102:105], v[160:163], v[208:211], v[102:105]
	v_mfma_f32_16x16x32_bf16 v[94:97], v[168:171], v[208:211], v[94:97]
	v_mfma_f32_16x16x32_bf16 v[86:89], v[160:163], v[216:219], v[86:89]
	v_mfma_f32_16x16x32_bf16 v[78:81], v[168:171], v[216:219], v[78:81]
	v_mfma_f32_16x16x32_bf16 v[114:117], v[172:175], v[188:191], v[114:117]
	v_mfma_f32_16x16x32_bf16 v[106:109], v[180:183], v[188:191], v[106:109]
	v_mfma_f32_16x16x32_bf16 v[98:101], v[172:175], v[196:199], v[98:101]
	v_mfma_f32_16x16x32_bf16 v[90:93], v[180:183], v[196:199], v[90:93]
	v_mfma_f32_16x16x32_bf16 v[82:85], v[172:175], v[204:207], v[82:85]
	v_mfma_f32_16x16x32_bf16 v[74:77], v[180:183], v[204:207], v[74:77]
	v_mfma_f32_16x16x32_bf16 v[70:73], v[172:175], v[212:215], v[70:73]
	v_mfma_f32_16x16x32_bf16 v[66:69], v[180:183], v[212:215], v[66:69]
	v_mfma_f32_16x16x32_bf16 v[114:117], v[176:179], v[192:195], v[114:117]
	v_mfma_f32_16x16x32_bf16 v[106:109], v[184:187], v[192:195], v[106:109]
	v_mfma_f32_16x16x32_bf16 v[98:101], v[176:179], v[200:203], v[98:101]
	v_mfma_f32_16x16x32_bf16 v[90:93], v[184:187], v[200:203], v[90:93]
	v_mfma_f32_16x16x32_bf16 v[82:85], v[176:179], v[208:211], v[82:85]
	v_mfma_f32_16x16x32_bf16 v[74:77], v[184:187], v[208:211], v[74:77]
	v_mfma_f32_16x16x32_bf16 v[70:73], v[176:179], v[216:219], v[70:73]
	v_mfma_f32_16x16x32_bf16 v[66:69], v[184:187], v[216:219], v[66:69]
	s_setprio 0
	s_barrier
	s_add_i32 s51, s42, s29
	v_lshl_add_u64 v[220:221], s[24:25], 0, v[134:135]
	s_mov_b32 m0, s51
	ds_read_b128 v[188:191], v158 offset:16384
	ds_read_b128 v[192:195], v158 offset:17408
	ds_read_b128 v[196:199], v158 offset:18432
	ds_read_b128 v[200:203], v158 offset:19456
	ds_read_b128 v[204:207], v158 offset:20480
	ds_read_b128 v[208:211], v158 offset:21504
	ds_read_b128 v[212:215], v158 offset:22528
	ds_read_b128 v[216:219], v158 offset:23552
	global_load_lds_dwordx4 v[220:221], off
	s_add_i32 m0, s51, 0x2000
	s_add_u32 s52, s24, 0x100000
	v_lshl_add_u64 v[222:223], s[24:25], 0, v[138:139]
	s_addc_u32 s53, s25, 0
	s_add_i32 s51, s43, s29
	global_load_lds_dwordx4 v[222:223], off
	v_lshl_add_u64 v[224:225], s[52:53], 0, v[134:135]
	s_mov_b32 m0, s51
	v_lshl_add_u64 v[226:227], s[26:27], 0, v[136:137]
	global_load_lds_dwordx4 v[224:225], off
	v_lshl_add_u64 v[224:225], s[52:53], 0, v[138:139]
	s_add_i32 m0, s51, 0x2000
	s_nop 0
	global_load_lds_dwordx4 v[224:225], off
	v_lshl_add_u64 v[224:225], s[26:27], 0, v[132:133]
	s_mov_b32 m0, s21
	s_nop 0
	global_load_lds_dwordx4 v[224:225], off
	s_mov_b32 m0, s35
	s_nop 0
	global_load_lds_dwordx4 v[226:227], off
	s_waitcnt vmcnt(8)
	s_waitcnt lgkmcnt(0)
	s_barrier
; #define PG8_STAGE(bufoff, gbase, voff) do { _Pragma("unroll") for (int _i = 0; _i < 2; ++_i) \
;         __builtin_amdgcn_global_load_lds((const unsigned*)((const char*)(gbase) + (voff)[_i]), (PG8_LAS unsigned*)(lds + (bufoff) + ldsw + _i * 8192), 16, 0, 0); } while (0)
; #define PG8_STAGE_A(bufoff, gb, vo, h) do { if constexpr (Sched::GATHER) { PG8_STAGE(bufoff, gb, (vo)[h]); } else { PG8_STAGE(bufoff, (gb) + (h) * hstep, voffA); } } while (0)
; #define PG8_LDA(dst, b, h) do { _Pragma("unroll") for (int m = 0; m < 4; ++m) _Pragma("unroll") for (int k = 0; k < 2; ++k) dst[m][k] = *(const PG8_LAS bf16x8*)(lds + PG8_SA(b, h) + aoff + m * 2048 + k * 1024); } while (0)
; #define PG8_LDB(dst, b, h) do { _Pragma("unroll") for (int n = 0; n < 2; ++n) _Pragma("unroll") for (int k = 0; k < 2; ++k) dst[n][k] = *(const PG8_LAS bf16x8*)(lds + PG8_SB(b, h) + boff + n * 2048 + k * 1024); } while (0)
; #define PG8_MMA(ai, bj, At, Bt) do { __builtin_amdgcn_s_setprio(1); _Pragma("unroll") for (int m = 0; m < 4; ++m) _Pragma("unroll") for (int n = 0; n < 2; ++n) _Pragma("unroll") for (int k = 0; k < 2; ++k) \
;         acc[ai][bj][m][n] = __builtin_amdgcn_mfma_f32_16x16x32_bf16(Bt[n][k], At[m][k], acc[ai][bj][m][n], 0, 0, 0); __builtin_amdgcn_s_setprio(0); } while (0)
; #define PG8_WAIT_V(n) asm volatile("s_waitcnt vmcnt(" #n ")" ::: "memory")
; #define PG8_WAIT_L(n) asm volatile("s_waitcnt lgkmcnt(" #n ")" ::: "memory")
; #define PG8_BAR __builtin_amdgcn_s_barrier()
; #define PG8_SCHED __builtin_amdgcn_sched_barrier(0)
; template <class Epi, class Sched, bool ALIGN_EPI>
; __device__ __forceinline__ void gemm_phase(PG8_LAS unsigned char* lds, const int K, const Sched& S, const Epi& E) {
;     ...
;             PG8_WAIT_V(8); PG8_WAIT_L(0); PG8_BAR; PG8_MMA(1, 0, At, B0); PG8_MMA(1, 1, At, B1); PG8_BAR; PG8_SCHED;
;             PG8_LDB(B0, 1, 0); PG8_LDB(B1, 1, 1); PG8_SCHED; PG8_LDA(At, 1, 0); PG8_STAGE_A(PG8_SA(0, 1), a2, vo2, 1);
;             PG8_WAIT_V(8); PG8_WAIT_L(0); PG8_BAR; PG8_MMA(0, 0, At, B0); PG8_MMA(0, 1, At, B1); PG8_BAR; PG8_SCHED;
;             PG8_LDA(At, 1, 1); PG8_STAGE(PG8_SB(1, 0), b3, voffB); PG8_STAGE(PG8_SB(1, 1), b3 + hstep, voffB); PG8_STAGE_A(PG8_SA(1, 0), a3, vo2, 0);
;             PG8_WAIT_V(8); PG8_WAIT_L(0); PG8_BAR; PG8_MMA(1, 0, At, B0); PG8_MMA(1, 1, At, B1); PG8_BAR; PG8_SCHED;
	s_setprio 1
	s_waitcnt lgkmcnt(0)
	v_mfma_f32_16x16x32_bf16 v[62:65], v[148:151], v[188:191], v[62:65]
	v_mfma_f32_16x16x32_bf16 v[58:61], v[164:167], v[188:191], v[58:61]
	v_mfma_f32_16x16x32_bf16 v[54:57], v[148:151], v[196:199], v[54:57]
	v_mfma_f32_16x16x32_bf16 v[46:49], v[164:167], v[196:199], v[46:49]
	v_mfma_f32_16x16x32_bf16 v[38:41], v[148:151], v[204:207], v[38:41]
	v_mfma_f32_16x16x32_bf16 v[30:33], v[164:167], v[204:207], v[30:33]
	v_mfma_f32_16x16x32_bf16 v[22:25], v[148:151], v[212:215], v[22:25]
	v_mfma_f32_16x16x32_bf16 v[14:17], v[164:167], v[212:215], v[14:17]
	v_mfma_f32_16x16x32_bf16 v[62:65], v[160:163], v[192:195], v[62:65]
	v_mfma_f32_16x16x32_bf16 v[58:61], v[168:171], v[192:195], v[58:61]
	v_mfma_f32_16x16x32_bf16 v[54:57], v[160:163], v[200:203], v[54:57]
	v_mfma_f32_16x16x32_bf16 v[46:49], v[168:171], v[200:203], v[46:49]
	v_mfma_f32_16x16x32_bf16 v[38:41], v[160:163], v[208:211], v[38:41]
	v_mfma_f32_16x16x32_bf16 v[30:33], v[168:171], v[208:211], v[30:33]
	v_mfma_f32_16x16x32_bf16 v[22:25], v[160:163], v[216:219], v[22:25]
	v_mfma_f32_16x16x32_bf16 v[14:17], v[168:171], v[216:219], v[14:17]
	v_mfma_f32_16x16x32_bf16 v[50:53], v[172:175], v[188:191], v[50:53]
	v_mfma_f32_16x16x32_bf16 v[42:45], v[180:183], v[188:191], v[42:45]
	v_mfma_f32_16x16x32_bf16 v[34:37], v[172:175], v[196:199], v[34:37]
	v_mfma_f32_16x16x32_bf16 v[26:29], v[180:183], v[196:199], v[26:29]
	v_mfma_f32_16x16x32_bf16 v[18:21], v[172:175], v[204:207], v[18:21]
	v_mfma_f32_16x16x32_bf16 v[10:13], v[180:183], v[204:207], v[10:13]
	v_mfma_f32_16x16x32_bf16 v[6:9], v[172:175], v[212:215], v[6:9]
	v_mfma_f32_16x16x32_bf16 v[2:5], v[180:183], v[212:215], v[2:5]
	v_mfma_f32_16x16x32_bf16 v[50:53], v[176:179], v[192:195], v[50:53]
	v_mfma_f32_16x16x32_bf16 v[42:45], v[184:187], v[192:195], v[42:45]
	v_mfma_f32_16x16x32_bf16 v[34:37], v[176:179], v[200:203], v[34:37]
	v_mfma_f32_16x16x32_bf16 v[26:29], v[184:187], v[200:203], v[26:29]
	v_mfma_f32_16x16x32_bf16 v[18:21], v[176:179], v[208:211], v[18:21]
	v_mfma_f32_16x16x32_bf16 v[10:13], v[184:187], v[208:211], v[10:13]
	v_mfma_f32_16x16x32_bf16 v[6:9], v[176:179], v[216:219], v[6:9]
	v_mfma_f32_16x16x32_bf16 v[2:5], v[184:187], v[216:219], v[2:5]
	s_setprio 0
	s_barrier
	s_add_i32 s51, 0, 0x18000
	v_add_u32_e32 v159, s51, v153
	s_add_i32 s52, 0, 0x1c000
	ds_read_b128 v[148:151], v159
	ds_read_b128 v[160:163], v159 offset:1024
	ds_read_b128 v[164:167], v159 offset:2048
	ds_read_b128 v[168:171], v159 offset:3072
	v_add_u32_e32 v159, s52, v153
	ds_read_b128 v[172:175], v159
	ds_read_b128 v[176:179], v159 offset:1024
	ds_read_b128 v[180:183], v159 offset:2048
	ds_read_b128 v[184:187], v159 offset:3072
	s_add_u32 s26, s26, 0x100000
	s_addc_u32 s27, s27, 0
	s_mov_b32 m0, s36
	v_lshl_add_u64 v[228:229], s[26:27], 0, v[132:133]
	ds_read_b128 v[188:191], v158 offset:32768
	ds_read_b128 v[192:195], v158 offset:33792
	ds_read_b128 v[196:199], v158 offset:34816
	ds_read_b128 v[200:203], v158 offset:35840
	ds_read_b128 v[204:207], v158 offset:36864
	ds_read_b128 v[208:211], v158 offset:37888
	ds_read_b128 v[212:215], v158 offset:38912
	ds_read_b128 v[216:219], v158 offset:39936
	global_load_lds_dwordx4 v[228:229], off
	v_lshl_add_u64 v[228:229], s[26:27], 0, v[136:137]
	s_mov_b32 m0, s37
	s_nop 0
	global_load_lds_dwordx4 v[228:229], off
	s_waitcnt vmcnt(8)
	s_waitcnt lgkmcnt(0)
	s_barrier
	s_setprio 1
	s_waitcnt lgkmcnt(0)
	v_mfma_f32_16x16x32_bf16 v[126:129], v[148:151], v[188:191], v[126:129]
	v_mfma_f32_16x16x32_bf16 v[122:125], v[164:167], v[188:191], v[122:125]
	v_mfma_f32_16x16x32_bf16 v[118:121], v[148:151], v[196:199], v[118:121]
	v_mfma_f32_16x16x32_bf16 v[110:113], v[164:167], v[196:199], v[110:113]
	v_mfma_f32_16x16x32_bf16 v[102:105], v[148:151], v[204:207], v[102:105]
	v_mfma_f32_16x16x32_bf16 v[94:97], v[164:167], v[204:207], v[94:97]
	v_mfma_f32_16x16x32_bf16 v[86:89], v[148:151], v[212:215], v[86:89]
	v_mfma_f32_16x16x32_bf16 v[78:81], v[164:167], v[212:215], v[78:81]
	v_mfma_f32_16x16x32_bf16 v[126:129], v[160:163], v[192:195], v[126:129]
	v_mfma_f32_16x16x32_bf16 v[122:125], v[168:171], v[192:195], v[122:125]
	v_mfma_f32_16x16x32_bf16 v[118:121], v[160:163], v[200:203], v[118:121]
	v_mfma_f32_16x16x32_bf16 v[110:113], v[168:171], v[200:203], v[110:113]
	v_mfma_f32_16x16x32_bf16 v[102:105], v[160:163], v[208:211], v[102:105]
	v_mfma_f32_16x16x32_bf16 v[94:97], v[168:171], v[208:211], v[94:97]
	v_mfma_f32_16x16x32_bf16 v[86:89], v[160:163], v[216:219], v[86:89]
	v_mfma_f32_16x16x32_bf16 v[78:81], v[168:171], v[216:219], v[78:81]
	v_mfma_f32_16x16x32_bf16 v[114:117], v[172:175], v[188:191], v[114:117]
	v_mfma_f32_16x16x32_bf16 v[106:109], v[180:183], v[188:191], v[106:109]
	v_mfma_f32_16x16x32_bf16 v[98:101], v[172:175], v[196:199], v[98:101]
	v_mfma_f32_16x16x32_bf16 v[90:93], v[180:183], v[196:199], v[90:93]
	v_mfma_f32_16x16x32_bf16 v[82:85], v[172:175], v[204:207], v[82:85]
	v_mfma_f32_16x16x32_bf16 v[74:77], v[180:183], v[204:207], v[74:77]
	v_mfma_f32_16x16x32_bf16 v[70:73], v[172:175], v[212:215], v[70:73]
	v_mfma_f32_16x16x32_bf16 v[66:69], v[180:183], v[212:215], v[66:69]
	v_mfma_f32_16x16x32_bf16 v[114:117], v[176:179], v[192:195], v[114:117]
	v_mfma_f32_16x16x32_bf16 v[106:109], v[184:187], v[192:195], v[106:109]
	v_mfma_f32_16x16x32_bf16 v[98:101], v[176:179], v[200:203], v[98:101]
	v_mfma_f32_16x16x32_bf16 v[90:93], v[184:187], v[200:203], v[90:93]
	v_mfma_f32_16x16x32_bf16 v[82:85], v[176:179], v[208:211], v[82:85]
	v_mfma_f32_16x16x32_bf16 v[74:77], v[184:187], v[208:211], v[74:77]
	v_mfma_f32_16x16x32_bf16 v[70:73], v[176:179], v[216:219], v[70:73]
	v_mfma_f32_16x16x32_bf16 v[66:69], v[184:187], v[216:219], v[66:69]
	s_setprio 0
	s_barrier
; #define PG8_STAGE(bufoff, gbase, voff) do { _Pragma("unroll") for (int _i = 0; _i < 2; ++_i) \
;         __builtin_amdgcn_global_load_lds((const unsigned*)((const char*)(gbase) + (voff)[_i]), (PG8_LAS unsigned*)(lds + (bufoff) + ldsw + _i * 8192), 16, 0, 0); } while (0)
; #define PG8_STAGE_A(bufoff, gb, vo, h) do { if constexpr (Sched::GATHER) { PG8_STAGE(bufoff, gb, (vo)[h]); } else { PG8_STAGE(bufoff, (gb) + (h) * hstep, voffA); } } while (0)
; #define PG8_LDA(dst, b, h) do { _Pragma("unroll") for (int m = 0; m < 4; ++m) _Pragma("unroll") for (int k = 0; k < 2; ++k) dst[m][k] = *(const PG8_LAS bf16x8*)(lds + PG8_SA(b, h) + aoff + m * 2048 + k * 1024); } while (0)
; #define PG8_MMA(ai, bj, At, Bt) do { __builtin_amdgcn_s_setprio(1); _Pragma("unroll") for (int m = 0; m < 4; ++m) _Pragma("unroll") for (int n = 0; n < 2; ++n) _Pragma("unroll") for (int k = 0; k < 2; ++k) \
;         acc[ai][bj][m][n] = __builtin_amdgcn_mfma_f32_16x16x32_bf16(Bt[n][k], At[m][k], acc[ai][bj][m][n], 0, 0, 0); __builtin_amdgcn_s_setprio(0); } while (0)
; #define PG8_WAIT_V(n) asm volatile("s_waitcnt vmcnt(" #n ")" ::: "memory")
; #define PG8_WAIT_L(n) asm volatile("s_waitcnt lgkmcnt(" #n ")" ::: "memory")
; #define PG8_BAR __builtin_amdgcn_s_barrier()
; #define PG8_SCHED __builtin_amdgcn_sched_barrier(0)
; template <class Epi, class Sched, bool ALIGN_EPI>
; __device__ __forceinline__ void gemm_phase(PG8_LAS unsigned char* lds, const int K, const Sched& S, const Epi& E) {
;     ...
;             PG8_LDA(At, 1, 1); PG8_STAGE(PG8_SB(1, 0), b3, voffB); PG8_STAGE(PG8_SB(1, 1), b3 + hstep, voffB); PG8_STAGE_A(PG8_SA(1, 0), a3, vo2, 0);
;             PG8_WAIT_V(8); PG8_WAIT_L(0); PG8_BAR; PG8_MMA(1, 0, At, B0); PG8_MMA(1, 1, At, B1); PG8_BAR; PG8_SCHED;
;         }
;         if constexpr (ALIGN_EPI) { if (wr == 0) PG8_BAR; }
	s_add_i32 s26, s51, s29
	v_lshl_add_u64 v[220:221], v[220:221], 0, s[8:9]
	s_mov_b32 m0, s26
	ds_read_b128 v[188:191], v158 offset:49152
	ds_read_b128 v[192:195], v158 offset:50176
	ds_read_b128 v[196:199], v158 offset:51200
	ds_read_b128 v[200:203], v158 offset:52224
	ds_read_b128 v[204:207], v158 offset:53248
	ds_read_b128 v[208:211], v158 offset:54272
	ds_read_b128 v[212:215], v158 offset:55296
	ds_read_b128 v[216:219], v158 offset:56320
	global_load_lds_dwordx4 v[220:221], off
	s_add_i32 m0, s26, 0x2000
	s_add_u32 s24, s24, 0x100080
	v_lshl_add_u64 v[220:221], v[222:223], 0, s[8:9]
	s_addc_u32 s25, s25, 0
	s_add_i32 s26, s52, s29
	global_load_lds_dwordx4 v[220:221], off
	v_lshl_add_u64 v[220:221], s[24:25], 0, v[134:135]
	s_mov_b32 m0, s26
	s_nop 0
	global_load_lds_dwordx4 v[220:221], off
	v_lshl_add_u64 v[220:221], s[24:25], 0, v[138:139]
	s_add_i32 m0, s26, 0x2000
	s_nop 0
	global_load_lds_dwordx4 v[220:221], off
	v_lshl_add_u64 v[220:221], v[224:225], 0, s[8:9]
	s_mov_b32 m0, s40
	s_nop 0
	global_load_lds_dwordx4 v[220:221], off
	v_lshl_add_u64 v[220:221], v[226:227], 0, s[8:9]
	s_mov_b32 m0, s41
	s_nop 0
	global_load_lds_dwordx4 v[220:221], off
	s_waitcnt vmcnt(8)
	s_waitcnt lgkmcnt(0)
	s_barrier
	s_setprio 1
	s_waitcnt lgkmcnt(0)
	v_mfma_f32_16x16x32_bf16 v[62:65], v[148:151], v[188:191], v[62:65]
	v_mfma_f32_16x16x32_bf16 v[58:61], v[164:167], v[188:191], v[58:61]
	v_mfma_f32_16x16x32_bf16 v[54:57], v[148:151], v[196:199], v[54:57]
	v_mfma_f32_16x16x32_bf16 v[46:49], v[164:167], v[196:199], v[46:49]
	v_mfma_f32_16x16x32_bf16 v[38:41], v[148:151], v[204:207], v[38:41]
	v_mfma_f32_16x16x32_bf16 v[30:33], v[164:167], v[204:207], v[30:33]
	v_mfma_f32_16x16x32_bf16 v[22:25], v[148:151], v[212:215], v[22:25]
	v_mfma_f32_16x16x32_bf16 v[14:17], v[164:167], v[212:215], v[14:17]
	v_mfma_f32_16x16x32_bf16 v[62:65], v[160:163], v[192:195], v[62:65]
	v_mfma_f32_16x16x32_bf16 v[58:61], v[168:171], v[192:195], v[58:61]
	v_mfma_f32_16x16x32_bf16 v[54:57], v[160:163], v[200:203], v[54:57]
	v_mfma_f32_16x16x32_bf16 v[46:49], v[168:171], v[200:203], v[46:49]
	v_mfma_f32_16x16x32_bf16 v[38:41], v[160:163], v[208:211], v[38:41]
	v_mfma_f32_16x16x32_bf16 v[30:33], v[168:171], v[208:211], v[30:33]
	v_mfma_f32_16x16x32_bf16 v[22:25], v[160:163], v[216:219], v[22:25]
	v_mfma_f32_16x16x32_bf16 v[14:17], v[168:171], v[216:219], v[14:17]
	v_mfma_f32_16x16x32_bf16 v[50:53], v[172:175], v[188:191], v[50:53]
	v_mfma_f32_16x16x32_bf16 v[42:45], v[180:183], v[188:191], v[42:45]
	v_mfma_f32_16x16x32_bf16 v[34:37], v[172:175], v[196:199], v[34:37]
	v_mfma_f32_16x16x32_bf16 v[26:29], v[180:183], v[196:199], v[26:29]
	v_mfma_f32_16x16x32_bf16 v[18:21], v[172:175], v[204:207], v[18:21]
	v_mfma_f32_16x16x32_bf16 v[10:13], v[180:183], v[204:207], v[10:13]
	v_mfma_f32_16x16x32_bf16 v[6:9], v[172:175], v[212:215], v[6:9]
	v_mfma_f32_16x16x32_bf16 v[2:5], v[180:183], v[212:215], v[2:5]
	v_mfma_f32_16x16x32_bf16 v[50:53], v[176:179], v[192:195], v[50:53]
	v_mfma_f32_16x16x32_bf16 v[42:45], v[184:187], v[192:195], v[42:45]
	v_mfma_f32_16x16x32_bf16 v[34:37], v[176:179], v[200:203], v[34:37]
	v_mfma_f32_16x16x32_bf16 v[26:29], v[184:187], v[200:203], v[26:29]
	v_mfma_f32_16x16x32_bf16 v[18:21], v[176:179], v[208:211], v[18:21]
	v_mfma_f32_16x16x32_bf16 v[10:13], v[184:187], v[208:211], v[10:13]
	v_mfma_f32_16x16x32_bf16 v[6:9], v[176:179], v[216:219], v[6:9]
	v_mfma_f32_16x16x32_bf16 v[2:5], v[184:187], v[216:219], v[2:5]
	s_setprio 0
	s_barrier
	s_add_i32 s50, s50, 2
	s_add_u32 s22, s22, 0x100
	s_addc_u32 s23, s23, 0
	s_add_u32 s48, s48, 0x100
	s_addc_u32 s49, s49, 0
	s_cmp_gt_u32 s50, 61
	s_cbranch_scc0 .LBB0_199
	s_and_b64 vcc, exec, s[10:11]
	s_cbranch_vccz .LBB0_202
	s_barrier

; #define PG8_STAGE(bufoff, gbase, voff) do { _Pragma("unroll") for (int _i = 0; _i < 2; ++_i) \
;         __builtin_amdgcn_global_load_lds((const unsigned*)((const char*)(gbase) + (voff)[_i]), (PG8_LAS unsigned*)(lds + (bufoff) + ldsw + _i * 8192), 16, 0, 0); } while (0)
; #define PG8_STAGE_A(bufoff, gb, vo, h) do { if constexpr (Sched::GATHER) { PG8_STAGE(bufoff, gb, (vo)[h]); } else { PG8_STAGE(bufoff, (gb) + (h) * hstep, voffA); } } while (0)
; #define PG8_LDA(dst, b, h) do { _Pragma("unroll") for (int m = 0; m < 4; ++m) _Pragma("unroll") for (int k = 0; k < 2; ++k) dst[m][k] = *(const PG8_LAS bf16x8*)(lds + PG8_SA(b, h) + aoff + m * 2048 + k * 1024); } while (0)
; #define PG8_LDB(dst, b, h) do { _Pragma("unroll") for (int n = 0; n < 2; ++n) _Pragma("unroll") for (int k = 0; k < 2; ++k) dst[n][k] = *(const PG8_LAS bf16x8*)(lds + PG8_SB(b, h) + boff + n * 2048 + k * 1024); } while (0)
; #define PG8_MMA(ai, bj, At, Bt) do { __builtin_amdgcn_s_setprio(1); _Pragma("unroll") for (int m = 0; m < 4; ++m) _Pragma("unroll") for (int n = 0; n < 2; ++n) _Pragma("unroll") for (int k = 0; k < 2; ++k) \
;         acc[ai][bj][m][n] = __builtin_amdgcn_mfma_f32_16x16x32_bf16(Bt[n][k], At[m][k], acc[ai][bj][m][n], 0, 0, 0); __builtin_amdgcn_s_setprio(0); } while (0)
; #define PG8_WAIT_V(n) asm volatile("s_waitcnt vmcnt(" #n ")" ::: "memory")
; #define PG8_WAIT_L(n) asm volatile("s_waitcnt lgkmcnt(" #n ")" ::: "memory")
; #define PG8_BAR __builtin_amdgcn_s_barrier()
; #define PG8_SCHED __builtin_amdgcn_sched_barrier(0)
; template <class Epi, class Sched, bool ALIGN_EPI>
; __device__ __forceinline__ void gemm_phase(PG8_LAS unsigned char* lds, const int K, const Sched& S, const Epi& E) {
;     ...
;             PG8_LDB(B0, 0, 0); PG8_LDB(B1, 0, 1); PG8_SCHED; PG8_LDA(At, 0, 0); PG8_STAGE_A(PG8_SA(1, 1), a1, cvo, 1);
;             PG8_WAIT_V(8); PG8_WAIT_L(0); PG8_BAR; PG8_MMA(0, 0, At, B0); PG8_MMA(0, 1, At, B1); PG8_BAR; PG8_SCHED;
;             PG8_LDA(At, 0, 1); PG8_STAGE(PG8_SB(0, 0), b2, voffB); PG8_STAGE(PG8_SB(0, 1), b2 + hstep, voffB); PG8_STAGE_A(PG8_SA(0, 0), a2, vo2, 0);
;             PG8_WAIT_V(8); PG8_WAIT_L(0); PG8_BAR; PG8_MMA(1, 0, At, B0); PG8_MMA(1, 1, At, B1); PG8_BAR; PG8_SCHED;
.LBB0_542:
	ds_read_b128 v[148:151], v158
	ds_read_b128 v[162:165], v158 offset:1024
	ds_read_b128 v[170:173], v158 offset:2048
	ds_read_b128 v[174:177], v158 offset:3072
	ds_read_b128 v[178:181], v159
	ds_read_b128 v[182:185], v159 offset:1024
	ds_read_b128 v[186:189], v159 offset:2048
	ds_read_b128 v[190:193], v159 offset:3072
	s_add_u32 s36, s34, 0xfff00080
	s_addc_u32 s37, s35, -1
	s_cmp_eq_u32 s58, 60
	s_cselect_b32 s39, s25, s37
	s_cselect_b32 s38, s54, s36
	s_cselect_b32 s37, s23, s57
	s_cselect_b32 s36, s55, s56
	v_lshl_add_u64 v[152:153], s[34:35], 0, v[140:141]
	s_add_i32 m0, s31, 0xc000
	ds_read_b128 v[194:197], v160
	ds_read_b128 v[198:201], v160 offset:1024
	ds_read_b128 v[202:205], v160 offset:2048
	ds_read_b128 v[206:209], v160 offset:3072
	ds_read_b128 v[210:213], v160 offset:4096
	ds_read_b128 v[214:217], v160 offset:5120
	ds_read_b128 v[218:221], v160 offset:6144
	ds_read_b128 v[222:225], v160 offset:7168
	global_load_lds_dwordx4 v[152:153], off
	v_lshl_add_u64 v[152:153], s[34:35], 0, v[142:143]
	s_add_i32 m0, s31, 0xe000
	s_nop 0
	global_load_lds_dwordx4 v[152:153], off
	s_waitcnt vmcnt(8)
	s_waitcnt lgkmcnt(0)
	s_barrier
	s_setprio 1
	s_waitcnt lgkmcnt(0)
	v_mfma_f32_16x16x32_bf16 v[126:129], v[148:151], v[194:197], v[126:129]
	v_mfma_f32_16x16x32_bf16 v[122:125], v[170:173], v[194:197], v[122:125]
	v_mfma_f32_16x16x32_bf16 v[110:113], v[148:151], v[202:205], v[110:113]
	v_mfma_f32_16x16x32_bf16 v[106:109], v[170:173], v[202:205], v[106:109]
	v_mfma_f32_16x16x32_bf16 v[94:97], v[148:151], v[210:213], v[94:97]
	v_mfma_f32_16x16x32_bf16 v[90:93], v[170:173], v[210:213], v[90:93]
	v_mfma_f32_16x16x32_bf16 v[78:81], v[148:151], v[218:221], v[78:81]
	v_mfma_f32_16x16x32_bf16 v[74:77], v[170:173], v[218:221], v[74:77]
	v_mfma_f32_16x16x32_bf16 v[126:129], v[162:165], v[198:201], v[126:129]
	v_mfma_f32_16x16x32_bf16 v[122:125], v[174:177], v[198:201], v[122:125]
	v_mfma_f32_16x16x32_bf16 v[110:113], v[162:165], v[206:209], v[110:113]
	v_mfma_f32_16x16x32_bf16 v[106:109], v[174:177], v[206:209], v[106:109]
	v_mfma_f32_16x16x32_bf16 v[94:97], v[162:165], v[214:217], v[94:97]
	v_mfma_f32_16x16x32_bf16 v[90:93], v[174:177], v[214:217], v[90:93]
	v_mfma_f32_16x16x32_bf16 v[78:81], v[162:165], v[222:225], v[78:81]
	v_mfma_f32_16x16x32_bf16 v[74:77], v[174:177], v[222:225], v[74:77]
	v_mfma_f32_16x16x32_bf16 v[118:121], v[178:181], v[194:197], v[118:121]
	v_mfma_f32_16x16x32_bf16 v[114:117], v[186:189], v[194:197], v[114:117]
	v_mfma_f32_16x16x32_bf16 v[102:105], v[178:181], v[202:205], v[102:105]
	v_mfma_f32_16x16x32_bf16 v[98:101], v[186:189], v[202:205], v[98:101]
	v_mfma_f32_16x16x32_bf16 v[86:89], v[178:181], v[210:213], v[86:89]
	v_mfma_f32_16x16x32_bf16 v[82:85], v[186:189], v[210:213], v[82:85]
	v_mfma_f32_16x16x32_bf16 v[70:73], v[178:181], v[218:221], v[70:73]
	v_mfma_f32_16x16x32_bf16 v[66:69], v[186:189], v[218:221], v[66:69]
	v_mfma_f32_16x16x32_bf16 v[118:121], v[182:185], v[198:201], v[118:121]
	v_mfma_f32_16x16x32_bf16 v[114:117], v[190:193], v[198:201], v[114:117]
	v_mfma_f32_16x16x32_bf16 v[102:105], v[182:185], v[206:209], v[102:105]
	v_mfma_f32_16x16x32_bf16 v[98:101], v[190:193], v[206:209], v[98:101]
	v_mfma_f32_16x16x32_bf16 v[86:89], v[182:185], v[214:217], v[86:89]
	v_mfma_f32_16x16x32_bf16 v[82:85], v[190:193], v[214:217], v[82:85]
	v_mfma_f32_16x16x32_bf16 v[70:73], v[182:185], v[222:225], v[70:73]
	v_mfma_f32_16x16x32_bf16 v[66:69], v[190:193], v[222:225], v[66:69]
	s_setprio 0
	s_barrier
	s_add_i32 s59, s51, s40
	v_lshl_add_u64 v[152:153], s[36:37], 0, v[134:135]
	s_mov_b32 m0, s59
	ds_read_b128 v[194:197], v160 offset:16384
	ds_read_b128 v[198:201], v160 offset:17408
	ds_read_b128 v[202:205], v160 offset:18432
	ds_read_b128 v[206:209], v160 offset:19456
	ds_read_b128 v[210:213], v160 offset:20480
	ds_read_b128 v[214:217], v160 offset:21504
	ds_read_b128 v[218:221], v160 offset:22528
	ds_read_b128 v[222:225], v160 offset:23552
	global_load_lds_dwordx4 v[152:153], off
	s_add_i32 m0, s59, 0x2000
	s_add_u32 s60, s36, 0x100000
	v_lshl_add_u64 v[166:167], s[36:37], 0, v[138:139]
	s_addc_u32 s61, s37, 0
	s_add_i32 s59, s52, s40
	global_load_lds_dwordx4 v[166:167], off
	v_lshl_add_u64 v[226:227], s[60:61], 0, v[134:135]
	s_mov_b32 m0, s59
	v_lshl_add_u64 v[228:229], s[38:39], 0, v[136:137]
	global_load_lds_dwordx4 v[226:227], off
	v_lshl_add_u64 v[226:227], s[60:61], 0, v[138:139]
	s_add_i32 m0, s59, 0x2000
	s_nop 0
	global_load_lds_dwordx4 v[226:227], off
	v_lshl_add_u64 v[226:227], s[38:39], 0, v[132:133]
	s_mov_b32 m0, s31
	s_nop 0
	global_load_lds_dwordx4 v[226:227], off
	s_mov_b32 m0, s44
	s_nop 0
	global_load_lds_dwordx4 v[228:229], off
	s_waitcnt vmcnt(8)
	s_waitcnt lgkmcnt(0)
	s_barrier
; #define PG8_STAGE(bufoff, gbase, voff) do { _Pragma("unroll") for (int _i = 0; _i < 2; ++_i) \
;         __builtin_amdgcn_global_load_lds((const unsigned*)((const char*)(gbase) + (voff)[_i]), (PG8_LAS unsigned*)(lds + (bufoff) + ldsw + _i * 8192), 16, 0, 0); } while (0)
; #define PG8_STAGE_A(bufoff, gb, vo, h) do { if constexpr (Sched::GATHER) { PG8_STAGE(bufoff, gb, (vo)[h]); } else { PG8_STAGE(bufoff, (gb) + (h) * hstep, voffA); } } while (0)
; #define PG8_LDA(dst, b, h) do { _Pragma("unroll") for (int m = 0; m < 4; ++m) _Pragma("unroll") for (int k = 0; k < 2; ++k) dst[m][k] = *(const PG8_LAS bf16x8*)(lds + PG8_SA(b, h) + aoff + m * 2048 + k * 1024); } while (0)
; #define PG8_LDB(dst, b, h) do { _Pragma("unroll") for (int n = 0; n < 2; ++n) _Pragma("unroll") for (int k = 0; k < 2; ++k) dst[n][k] = *(const PG8_LAS bf16x8*)(lds + PG8_SB(b, h) + boff + n * 2048 + k * 1024); } while (0)
; #define PG8_MMA(ai, bj, At, Bt) do { __builtin_amdgcn_s_setprio(1); _Pragma("unroll") for (int m = 0; m < 4; ++m) _Pragma("unroll") for (int n = 0; n < 2; ++n) _Pragma("unroll") for (int k = 0; k < 2; ++k) \
;         acc[ai][bj][m][n] = __builtin_amdgcn_mfma_f32_16x16x32_bf16(Bt[n][k], At[m][k], acc[ai][bj][m][n], 0, 0, 0); __builtin_amdgcn_s_setprio(0); } while (0)
; #define PG8_WAIT_V(n) asm volatile("s_waitcnt vmcnt(" #n ")" ::: "memory")
; #define PG8_WAIT_L(n) asm volatile("s_waitcnt lgkmcnt(" #n ")" ::: "memory")
; #define PG8_BAR __builtin_amdgcn_s_barrier()
; #define PG8_SCHED __builtin_amdgcn_sched_barrier(0)
; template <class Epi, class Sched, bool ALIGN_EPI>
; __device__ __forceinline__ void gemm_phase(PG8_LAS unsigned char* lds, const int K, const Sched& S, const Epi& E) {
;     ...
;             PG8_WAIT_V(8); PG8_WAIT_L(0); PG8_BAR; PG8_MMA(1, 0, At, B0); PG8_MMA(1, 1, At, B1); PG8_BAR; PG8_SCHED;
;             PG8_LDB(B0, 1, 0); PG8_LDB(B1, 1, 1); PG8_SCHED; PG8_LDA(At, 1, 0); PG8_STAGE_A(PG8_SA(0, 1), a2, vo2, 1);
;             PG8_WAIT_V(8); PG8_WAIT_L(0); PG8_BAR; PG8_MMA(0, 0, At, B0); PG8_MMA(0, 1, At, B1); PG8_BAR; PG8_SCHED;
;             PG8_LDA(At, 1, 1); PG8_STAGE(PG8_SB(1, 0), b3, voffB); PG8_STAGE(PG8_SB(1, 1), b3 + hstep, voffB); PG8_STAGE_A(PG8_SA(1, 0), a3, vo2, 0);
;             PG8_WAIT_V(8); PG8_WAIT_L(0); PG8_BAR; PG8_MMA(1, 0, At, B0); PG8_MMA(1, 1, At, B1); PG8_BAR; PG8_SCHED;
	s_setprio 1
	s_waitcnt lgkmcnt(0)
	v_mfma_f32_16x16x32_bf16 v[62:65], v[148:151], v[194:197], v[62:65]
	v_mfma_f32_16x16x32_bf16 v[58:61], v[170:173], v[194:197], v[58:61]
	v_mfma_f32_16x16x32_bf16 v[46:49], v[148:151], v[202:205], v[46:49]
	v_mfma_f32_16x16x32_bf16 v[42:45], v[170:173], v[202:205], v[42:45]
	v_mfma_f32_16x16x32_bf16 v[30:33], v[148:151], v[210:213], v[30:33]
	v_mfma_f32_16x16x32_bf16 v[26:29], v[170:173], v[210:213], v[26:29]
	v_mfma_f32_16x16x32_bf16 v[14:17], v[148:151], v[218:221], v[14:17]
	v_mfma_f32_16x16x32_bf16 v[10:13], v[170:173], v[218:221], v[10:13]
	v_mfma_f32_16x16x32_bf16 v[62:65], v[162:165], v[198:201], v[62:65]
	v_mfma_f32_16x16x32_bf16 v[58:61], v[174:177], v[198:201], v[58:61]
	v_mfma_f32_16x16x32_bf16 v[46:49], v[162:165], v[206:209], v[46:49]
	v_mfma_f32_16x16x32_bf16 v[42:45], v[174:177], v[206:209], v[42:45]
	v_mfma_f32_16x16x32_bf16 v[30:33], v[162:165], v[214:217], v[30:33]
	v_mfma_f32_16x16x32_bf16 v[26:29], v[174:177], v[214:217], v[26:29]
	v_mfma_f32_16x16x32_bf16 v[14:17], v[162:165], v[222:225], v[14:17]
	v_mfma_f32_16x16x32_bf16 v[10:13], v[174:177], v[222:225], v[10:13]
	v_mfma_f32_16x16x32_bf16 v[54:57], v[178:181], v[194:197], v[54:57]
	v_mfma_f32_16x16x32_bf16 v[50:53], v[186:189], v[194:197], v[50:53]
	v_mfma_f32_16x16x32_bf16 v[38:41], v[178:181], v[202:205], v[38:41]
	v_mfma_f32_16x16x32_bf16 v[34:37], v[186:189], v[202:205], v[34:37]
	v_mfma_f32_16x16x32_bf16 v[22:25], v[178:181], v[210:213], v[22:25]
	v_mfma_f32_16x16x32_bf16 v[18:21], v[186:189], v[210:213], v[18:21]
	v_mfma_f32_16x16x32_bf16 v[6:9], v[178:181], v[218:221], v[6:9]
	v_mfma_f32_16x16x32_bf16 v[2:5], v[186:189], v[218:221], v[2:5]
	v_mfma_f32_16x16x32_bf16 v[54:57], v[182:185], v[198:201], v[54:57]
	v_mfma_f32_16x16x32_bf16 v[50:53], v[190:193], v[198:201], v[50:53]
	v_mfma_f32_16x16x32_bf16 v[38:41], v[182:185], v[206:209], v[38:41]
	v_mfma_f32_16x16x32_bf16 v[34:37], v[190:193], v[206:209], v[34:37]
	v_mfma_f32_16x16x32_bf16 v[22:25], v[182:185], v[214:217], v[22:25]
	v_mfma_f32_16x16x32_bf16 v[18:21], v[190:193], v[214:217], v[18:21]
	v_mfma_f32_16x16x32_bf16 v[6:9], v[182:185], v[222:225], v[6:9]
	v_mfma_f32_16x16x32_bf16 v[2:5], v[190:193], v[222:225], v[2:5]
	s_setprio 0
	s_barrier
	s_add_i32 s59, 0, 0x18000
	v_add_u32_e32 v161, s59, v156
	s_add_i32 s60, 0, 0x1c000
	ds_read_b128 v[148:151], v161
	ds_read_b128 v[162:165], v161 offset:1024
	ds_read_b128 v[170:173], v161 offset:2048
	ds_read_b128 v[174:177], v161 offset:3072
	v_add_u32_e32 v161, s60, v156
	ds_read_b128 v[178:181], v161
	ds_read_b128 v[182:185], v161 offset:1024
	ds_read_b128 v[186:189], v161 offset:2048
	ds_read_b128 v[190:193], v161 offset:3072
	s_add_u32 s38, s38, 0x100000
	s_addc_u32 s39, s39, 0
	s_mov_b32 m0, s45
	v_lshl_add_u64 v[230:231], s[38:39], 0, v[132:133]
	ds_read_b128 v[194:197], v160 offset:32768
	ds_read_b128 v[198:201], v160 offset:33792
	ds_read_b128 v[202:205], v160 offset:34816
	ds_read_b128 v[206:209], v160 offset:35840
	ds_read_b128 v[210:213], v160 offset:36864
	ds_read_b128 v[214:217], v160 offset:37888
	ds_read_b128 v[218:221], v160 offset:38912
	ds_read_b128 v[222:225], v160 offset:39936
	global_load_lds_dwordx4 v[230:231], off
	v_lshl_add_u64 v[230:231], s[38:39], 0, v[136:137]
	s_mov_b32 m0, s46
	s_nop 0
	global_load_lds_dwordx4 v[230:231], off
	s_waitcnt vmcnt(8)
	s_waitcnt lgkmcnt(0)
	s_barrier
	s_setprio 1
	s_waitcnt lgkmcnt(0)
	v_mfma_f32_16x16x32_bf16 v[126:129], v[148:151], v[194:197], v[126:129]
	v_mfma_f32_16x16x32_bf16 v[122:125], v[170:173], v[194:197], v[122:125]
	v_mfma_f32_16x16x32_bf16 v[110:113], v[148:151], v[202:205], v[110:113]
	v_mfma_f32_16x16x32_bf16 v[106:109], v[170:173], v[202:205], v[106:109]
	v_mfma_f32_16x16x32_bf16 v[94:97], v[148:151], v[210:213], v[94:97]
	v_mfma_f32_16x16x32_bf16 v[90:93], v[170:173], v[210:213], v[90:93]
	v_mfma_f32_16x16x32_bf16 v[78:81], v[148:151], v[218:221], v[78:81]
	v_mfma_f32_16x16x32_bf16 v[74:77], v[170:173], v[218:221], v[74:77]
	v_mfma_f32_16x16x32_bf16 v[126:129], v[162:165], v[198:201], v[126:129]
	v_mfma_f32_16x16x32_bf16 v[122:125], v[174:177], v[198:201], v[122:125]
	v_mfma_f32_16x16x32_bf16 v[110:113], v[162:165], v[206:209], v[110:113]
	v_mfma_f32_16x16x32_bf16 v[106:109], v[174:177], v[206:209], v[106:109]
	v_mfma_f32_16x16x32_bf16 v[94:97], v[162:165], v[214:217], v[94:97]
	v_mfma_f32_16x16x32_bf16 v[90:93], v[174:177], v[214:217], v[90:93]
	v_mfma_f32_16x16x32_bf16 v[78:81], v[162:165], v[222:225], v[78:81]
	v_mfma_f32_16x16x32_bf16 v[74:77], v[174:177], v[222:225], v[74:77]
	v_mfma_f32_16x16x32_bf16 v[118:121], v[178:181], v[194:197], v[118:121]
	v_mfma_f32_16x16x32_bf16 v[114:117], v[186:189], v[194:197], v[114:117]
	v_mfma_f32_16x16x32_bf16 v[102:105], v[178:181], v[202:205], v[102:105]
	v_mfma_f32_16x16x32_bf16 v[98:101], v[186:189], v[202:205], v[98:101]
	v_mfma_f32_16x16x32_bf16 v[86:89], v[178:181], v[210:213], v[86:89]
	v_mfma_f32_16x16x32_bf16 v[82:85], v[186:189], v[210:213], v[82:85]
	v_mfma_f32_16x16x32_bf16 v[70:73], v[178:181], v[218:221], v[70:73]
	v_mfma_f32_16x16x32_bf16 v[66:69], v[186:189], v[218:221], v[66:69]
	v_mfma_f32_16x16x32_bf16 v[118:121], v[182:185], v[198:201], v[118:121]
	v_mfma_f32_16x16x32_bf16 v[114:117], v[190:193], v[198:201], v[114:117]
	v_mfma_f32_16x16x32_bf16 v[102:105], v[182:185], v[206:209], v[102:105]
	v_mfma_f32_16x16x32_bf16 v[98:101], v[190:193], v[206:209], v[98:101]
	v_mfma_f32_16x16x32_bf16 v[86:89], v[182:185], v[214:217], v[86:89]
	v_mfma_f32_16x16x32_bf16 v[82:85], v[190:193], v[214:217], v[82:85]
	v_mfma_f32_16x16x32_bf16 v[70:73], v[182:185], v[222:225], v[70:73]
	v_mfma_f32_16x16x32_bf16 v[66:69], v[190:193], v[222:225], v[66:69]
	s_setprio 0
	s_barrier
; #define PG8_STAGE(bufoff, gbase, voff) do { _Pragma("unroll") for (int _i = 0; _i < 2; ++_i) \
;         __builtin_amdgcn_global_load_lds((const unsigned*)((const char*)(gbase) + (voff)[_i]), (PG8_LAS unsigned*)(lds + (bufoff) + ldsw + _i * 8192), 16, 0, 0); } while (0)
; #define PG8_STAGE_A(bufoff, gb, vo, h) do { if constexpr (Sched::GATHER) { PG8_STAGE(bufoff, gb, (vo)[h]); } else { PG8_STAGE(bufoff, (gb) + (h) * hstep, voffA); } } while (0)
; #define PG8_LDA(dst, b, h) do { _Pragma("unroll") for (int m = 0; m < 4; ++m) _Pragma("unroll") for (int k = 0; k < 2; ++k) dst[m][k] = *(const PG8_LAS bf16x8*)(lds + PG8_SA(b, h) + aoff + m * 2048 + k * 1024); } while (0)
; #define PG8_MMA(ai, bj, At, Bt) do { __builtin_amdgcn_s_setprio(1); _Pragma("unroll") for (int m = 0; m < 4; ++m) _Pragma("unroll") for (int n = 0; n < 2; ++n) _Pragma("unroll") for (int k = 0; k < 2; ++k) \
;         acc[ai][bj][m][n] = __builtin_amdgcn_mfma_f32_16x16x32_bf16(Bt[n][k], At[m][k], acc[ai][bj][m][n], 0, 0, 0); __builtin_amdgcn_s_setprio(0); } while (0)
; #define PG8_WAIT_V(n) asm volatile("s_waitcnt vmcnt(" #n ")" ::: "memory")
; #define PG8_WAIT_L(n) asm volatile("s_waitcnt lgkmcnt(" #n ")" ::: "memory")
; #define PG8_BAR __builtin_amdgcn_s_barrier()
; #define PG8_SCHED __builtin_amdgcn_sched_barrier(0)
; template <class Epi, class Sched, bool ALIGN_EPI>
; __device__ __forceinline__ void gemm_phase(PG8_LAS unsigned char* lds, const int K, const Sched& S, const Epi& E) {
;     ...
;             PG8_LDA(At, 1, 1); PG8_STAGE(PG8_SB(1, 0), b3, voffB); PG8_STAGE(PG8_SB(1, 1), b3 + hstep, voffB); PG8_STAGE_A(PG8_SA(1, 0), a3, vo2, 0);
;             PG8_WAIT_V(8); PG8_WAIT_L(0); PG8_BAR; PG8_MMA(1, 0, At, B0); PG8_MMA(1, 1, At, B1); PG8_BAR; PG8_SCHED;
;         }
;         if constexpr (ALIGN_EPI) { if (wr == 0) PG8_BAR; }
	s_add_i32 s38, s59, s40
	v_lshl_add_u64 v[152:153], v[152:153], 0, s[10:11]
	s_mov_b32 m0, s38
	ds_read_b128 v[194:197], v160 offset:49152
	ds_read_b128 v[198:201], v160 offset:50176
	ds_read_b128 v[202:205], v160 offset:51200
	ds_read_b128 v[206:209], v160 offset:52224
	ds_read_b128 v[210:213], v160 offset:53248
	ds_read_b128 v[214:217], v160 offset:54272
	ds_read_b128 v[218:221], v160 offset:55296
	ds_read_b128 v[222:225], v160 offset:56320
	global_load_lds_dwordx4 v[152:153], off
	s_add_i32 m0, s38, 0x2000
	s_add_u32 s36, s36, 0x100080
	v_lshl_add_u64 v[152:153], v[166:167], 0, s[10:11]
	s_addc_u32 s37, s37, 0
	s_add_i32 s38, s60, s40
	global_load_lds_dwordx4 v[152:153], off
	v_lshl_add_u64 v[152:153], s[36:37], 0, v[134:135]
	s_mov_b32 m0, s38
	s_nop 0
	global_load_lds_dwordx4 v[152:153], off
	v_lshl_add_u64 v[152:153], s[36:37], 0, v[138:139]
	s_add_i32 m0, s38, 0x2000
	s_nop 0
	global_load_lds_dwordx4 v[152:153], off
	v_lshl_add_u64 v[152:153], v[226:227], 0, s[10:11]
	s_mov_b32 m0, s49
	s_nop 0
	global_load_lds_dwordx4 v[152:153], off
	v_lshl_add_u64 v[152:153], v[228:229], 0, s[10:11]
	s_mov_b32 m0, s50
	s_nop 0
	global_load_lds_dwordx4 v[152:153], off
	s_waitcnt vmcnt(8)
	s_waitcnt lgkmcnt(0)
	s_barrier
	s_setprio 1
	s_waitcnt lgkmcnt(0)
	v_mfma_f32_16x16x32_bf16 v[62:65], v[148:151], v[194:197], v[62:65]
	v_mfma_f32_16x16x32_bf16 v[58:61], v[170:173], v[194:197], v[58:61]
	v_mfma_f32_16x16x32_bf16 v[46:49], v[148:151], v[202:205], v[46:49]
	v_mfma_f32_16x16x32_bf16 v[42:45], v[170:173], v[202:205], v[42:45]
	v_mfma_f32_16x16x32_bf16 v[30:33], v[148:151], v[210:213], v[30:33]
	v_mfma_f32_16x16x32_bf16 v[26:29], v[170:173], v[210:213], v[26:29]
	v_mfma_f32_16x16x32_bf16 v[14:17], v[148:151], v[218:221], v[14:17]
	v_mfma_f32_16x16x32_bf16 v[10:13], v[170:173], v[218:221], v[10:13]
	v_mfma_f32_16x16x32_bf16 v[62:65], v[162:165], v[198:201], v[62:65]
	v_mfma_f32_16x16x32_bf16 v[58:61], v[174:177], v[198:201], v[58:61]
	v_mfma_f32_16x16x32_bf16 v[46:49], v[162:165], v[206:209], v[46:49]
	v_mfma_f32_16x16x32_bf16 v[42:45], v[174:177], v[206:209], v[42:45]
	v_mfma_f32_16x16x32_bf16 v[30:33], v[162:165], v[214:217], v[30:33]
	v_mfma_f32_16x16x32_bf16 v[26:29], v[174:177], v[214:217], v[26:29]
	v_mfma_f32_16x16x32_bf16 v[14:17], v[162:165], v[222:225], v[14:17]
	v_mfma_f32_16x16x32_bf16 v[10:13], v[174:177], v[222:225], v[10:13]
	v_mfma_f32_16x16x32_bf16 v[54:57], v[178:181], v[194:197], v[54:57]
	v_mfma_f32_16x16x32_bf16 v[50:53], v[186:189], v[194:197], v[50:53]
	v_mfma_f32_16x16x32_bf16 v[38:41], v[178:181], v[202:205], v[38:41]
	v_mfma_f32_16x16x32_bf16 v[34:37], v[186:189], v[202:205], v[34:37]
	v_mfma_f32_16x16x32_bf16 v[22:25], v[178:181], v[210:213], v[22:25]
	v_mfma_f32_16x16x32_bf16 v[18:21], v[186:189], v[210:213], v[18:21]
	v_mfma_f32_16x16x32_bf16 v[6:9], v[178:181], v[218:221], v[6:9]
	v_mfma_f32_16x16x32_bf16 v[2:5], v[186:189], v[218:221], v[2:5]
	v_mfma_f32_16x16x32_bf16 v[54:57], v[182:185], v[198:201], v[54:57]
	v_mfma_f32_16x16x32_bf16 v[50:53], v[190:193], v[198:201], v[50:53]
	v_mfma_f32_16x16x32_bf16 v[38:41], v[182:185], v[206:209], v[38:41]
	v_mfma_f32_16x16x32_bf16 v[34:37], v[190:193], v[206:209], v[34:37]
	v_mfma_f32_16x16x32_bf16 v[22:25], v[182:185], v[214:217], v[22:25]
	v_mfma_f32_16x16x32_bf16 v[18:21], v[190:193], v[214:217], v[18:21]
	v_mfma_f32_16x16x32_bf16 v[6:9], v[182:185], v[222:225], v[6:9]
	v_mfma_f32_16x16x32_bf16 v[2:5], v[190:193], v[222:225], v[2:5]
	s_setprio 0
	s_barrier
	s_add_i32 s58, s58, 2
	s_add_u32 s34, s34, 0x100
	s_addc_u32 s35, s35, 0
	s_add_u32 s56, s56, 0x100
	s_addc_u32 s57, s57, 0
	s_cmp_gt_u32 s58, 61
	s_cbranch_scc0 .LBB0_542
	s_and_b64 vcc, exec, s[12:13]
	s_cbranch_vccz .LBB0_545
	s_barrier
